# c17
# speedup vs baseline: 1.0016x; 1.0016x over previous
_Z6mxgemmILi0ELi1024ELi4EEvPKcS1_PKfS3_Pvi:
	s_load_dwordx8 s[4:11], s[0:1], 0x0
	s_lshr_b32 s13, s2, 3
	s_and_b32 s12, s2, 7
	s_lshl_b32 s12, s12, 7
	s_add_i32 s2, s12, s13
	v_readfirstlane_b32 s33, v0
	s_lshr_b32 s3, s2, 8
	s_and_b32 s2, s2, 0xff
	s_lshr_b32 s14, s2, 3
	s_and_b32 s2, s2, 7
	s_lshl_b32 s3, s3, 3
	s_add_i32 s2, s2, s3
	s_mov_b32 s15, 0
	s_mov_b32 s3, 0
	s_lshr_b32 s50, s33, 6
	s_lshr_b32 s29, s33, 8
	s_waitcnt lgkmcnt(0)
	s_lshl_b64 s[24:25], s[14:15], 17
	s_lshl_b64 s[44:45], s[2:3], 14
	s_add_u32 s3, s6, s44
	s_addc_u32 s12, s7, s45
	s_add_u32 s16, s3, 0xc00000
	s_mul_hi_u32 s3, s33, 0xaaaaaaab
	s_addc_u32 s17, s12, 0
	s_lshr_b32 s30, s3, 8
	s_mul_i32 s12, s30, -6
	s_lshl_b32 s28, s50, 10
	s_add_i32 s12, s12, s50
	s_lshr_b32 s13, s3, 9
	s_bitcmp1_b32 s3, 8
	s_cselect_b32 s34, 0x3000, 0
	s_lshl_b32 s3, s12, 10
	s_add_i32 s12, s50, 8
	s_mul_hi_u32 s35, s12, 0x2aaaaaab
	s_mul_i32 s31, s13, 0x6000
	s_add_i32 s52, s3, s34
	s_lshl_b32 s3, s13, 15
	s_mul_i32 s13, s35, -6
	s_add_i32 s18, s52, s31
	s_add_i32 s13, s13, s12
	s_lshr_b32 s41, s35, 1
	s_bitcmp1_b32 s35, 0
	s_cselect_b32 s37, 0x3000, 0
	s_add_i32 s12, s50, 16
	s_lshl_b32 s42, s13, 10
	s_mul_hi_u32 s38, s12, 0x2aaaaaab
	s_mul_i32 s36, s41, 0x6000
	s_add_i32 s42, s42, s37
	s_mul_i32 s13, s38, -6
	s_add_i32 s20, s42, s36
	s_add_i32 s13, s13, s12
	s_lshr_b32 s43, s38, 1
	s_bitcmp1_b32 s38, 0
	s_cselect_b32 s40, 0x3000, 0
	s_lshl_b32 s51, s13, 10
	s_mul_i32 s39, s43, 0x6000
	s_add_i32 s51, s51, s40
	s_mul_i32 s26, s2, 0x60000
	s_add_i32 s22, s51, s39
	s_mul_hi_i32 s27, s2, 0x60000
	s_add_u32 s12, s6, s26
	s_addc_u32 s13, s7, s27
	s_add_u32 s46, s4, s24
	s_addc_u32 s47, s5, s25
	s_add_i32 s52, s52, s3
	s_lshl_b32 s3, s41, 13
	s_add_i32 s3, s20, s3
	s_add_i32 s58, s3, 0
	s_lshl_b32 s3, s43, 13
	v_mov_b32_e32 v2, 0
	s_add_i32 s15, s28, 0
	s_add_i32 s3, s22, s3
	v_lshlrev_b32_e32 v4, 4, v0
	v_mov_b32_e32 v5, v2
	s_mov_b32 m0, s15
	s_add_i32 s59, s3, 0
	s_lshl_b32 s3, s50, 8
	v_lshl_add_u64 v[138:139], s[46:47], 0, v[4:5]
	global_load_lds_dwordx4 v4, s[46:47]
	s_mov_b64 s[46:47], 0x2000
	s_add_i32 s53, s52, 0
	s_add_i32 s3, s3, 0
	v_and_b32_e32 v1, 63, v0
	v_lshl_add_u64 v[8:9], v[138:139], 0, s[46:47]
	s_add_i32 s46, s15, 0x8000
	s_ashr_i32 s19, s18, 31
	s_add_i32 s47, s53, 0x2000
	s_ashr_i32 s21, s20, 31
	s_add_i32 s48, s58, 0x2000
	s_ashr_i32 s23, s22, 31
	s_add_i32 s49, s59, 0x2000
	s_add_i32 s50, s3, 0x20000
	v_lshlrev_b32_e32 v6, 4, v1
	v_mov_b32_e32 v7, v2
	s_add_u32 s54, s12, s18
	s_mov_b32 m0, s46
	v_lshl_add_u64 v[140:141], s[12:13], 0, v[6:7]
	s_addc_u32 s55, s13, s19
	s_addk_i32 s53, 0x3800
	global_load_lds_dwordx4 v[8:9], off
	v_lshl_add_u64 v[8:9], v[140:141], 0, s[18:19]
	s_mov_b32 m0, s47
	v_lshl_add_u64 v[132:133], s[54:55], 0, v[6:7]
	s_add_u32 s54, s12, s20
	global_load_lds_dwordx4 v[8:9], off
	v_lshl_add_u64 v[8:9], v[140:141], 0, s[20:21]
	s_mov_b32 m0, s48
	s_addc_u32 s55, s13, s21
	global_load_lds_dwordx4 v[8:9], off
	v_lshl_add_u64 v[8:9], v[140:141], 0, s[22:23]
	s_mov_b32 m0, s49
	v_lshl_add_u64 v[134:135], s[54:55], 0, v[6:7]
	s_add_i32 s55, s58, 0x3800
	v_lshlrev_b32_e32 v130, 2, v0
	global_load_lds_dwordx4 v[8:9], off
	s_mov_b32 m0, s50
	s_mov_b64 s[56:57], 0x1800
	s_add_u32 s12, s12, s22
	global_load_lds_dword v130, s[16:17]
	v_lshl_add_u64 v[8:9], v[132:133], 0, s[56:57]
	s_mov_b32 m0, s53
	s_addc_u32 s13, s13, s23
	global_load_lds_dwordx4 v[8:9], off
	v_lshl_add_u64 v[8:9], v[134:135], 0, s[56:57]
	s_mov_b32 m0, s55
	v_lshl_add_u64 v[136:137], s[12:13], 0, v[6:7]
	global_load_lds_dwordx4 v[8:9], off
	v_lshl_add_u64 v[8:9], v[136:137], 0, s[56:57]
	s_add_i32 s56, s59, 0x3800
	s_mov_b32 m0, s56
	s_load_dwordx2 s[12:13], s[0:1], 0x20
	global_load_lds_dwordx4 v[8:9], off
	s_mov_b64 s[70:71], 0x4000
	s_add_i32 m0, s28, 0x10000
	v_lshl_add_u64 v[8:9], v[138:139], 0, s[70:71]
	global_load_lds_dwordx4 v[8:9], off
	s_mov_b64 s[70:71], 0x6000
	s_add_i32 m0, s15, 0x18000
	v_lshl_add_u64 v[8:9], v[138:139], 0, s[70:71]
	global_load_lds_dwordx4 v[8:9], off
	s_cmp_lg_u32 s29, 1
	v_mov_b32_e32 v131, v2
	s_cbranch_scc1 .LBB2_2
	s_barrier

_Z6mxgemmILi1ELi4096ELi4EEvPKcS1_PKfS3_Pvi:
	s_load_dwordx4 s[4:7], s[0:1], 0x0
	s_load_dwordx2 s[10:11], s[0:1], 0x10
	s_lshr_b32 s9, s2, 3
	s_and_b32 s8, s2, 7
	s_lshl_b32 s8, s8, 6
	s_add_i32 s2, s8, s9
	v_readfirstlane_b32 s33, v0
	s_lshr_b32 s3, s2, 7
	s_and_b32 s2, s2, 0x7f
	s_lshr_b32 s12, s2, 3
	s_and_b32 s2, s2, 7
	s_lshl_b32 s8, s3, 3
	s_add_i32 s8, s8, s2
	s_mov_b32 s13, 0
	s_mov_b32 s9, 0
	s_lshr_b32 s48, s33, 6
	s_lshr_b32 s27, s33, 8
	s_waitcnt lgkmcnt(0)
	s_lshl_b64 s[22:23], s[12:13], 19
	s_lshl_b64 s[42:43], s[8:9], 16
	s_add_u32 s2, s6, s42
	s_addc_u32 s3, s7, s43
	s_add_u32 s14, s2, 0x3000000
	s_mul_hi_u32 s2, s33, 0xaaaaaaab
	s_addc_u32 s15, s3, 0
	s_lshr_b32 s28, s2, 8
	s_mul_i32 s3, s28, -6
	s_lshl_b32 s26, s48, 10
	s_add_i32 s3, s3, s48
	s_lshr_b32 s9, s2, 9
	s_bitcmp1_b32 s2, 8
	s_cselect_b32 s30, 0x3000, 0
	s_lshl_b32 s2, s3, 10
	s_add_i32 s50, s2, s30
	s_add_i32 s2, s48, 8
	s_mul_hi_u32 s31, s2, 0x2aaaaaab
	s_mul_i32 s29, s9, 0x6000
	s_mul_i32 s3, s31, -6
	s_add_i32 s16, s50, s29
	s_lshl_b32 s9, s9, 15
	s_add_i32 s3, s3, s2
	s_lshr_b32 s39, s31, 1
	s_bitcmp1_b32 s31, 0
	s_cselect_b32 s35, 0x3000, 0
	s_add_i32 s2, s48, 16
	s_lshl_b32 s40, s3, 10
	s_mul_hi_u32 s36, s2, 0x2aaaaaab
	s_mul_i32 s34, s39, 0x6000
	s_add_i32 s40, s40, s35
	s_mul_i32 s3, s36, -6
	s_add_i32 s18, s40, s34
	s_add_i32 s3, s3, s2
	s_lshr_b32 s41, s36, 1
	s_bitcmp1_b32 s36, 0
	s_cselect_b32 s38, 0x3000, 0
	s_lshl_b32 s49, s3, 10
	s_mul_i32 s37, s41, 0x6000
	s_add_i32 s49, s49, s38
	s_mul_i32 s24, s8, 0x180000
	s_add_i32 s20, s49, s37
	s_mul_hi_i32 s25, s8, 0x180000
	s_add_u32 s2, s6, s24
	s_addc_u32 s3, s7, s25
	s_add_u32 s44, s4, s22
	s_addc_u32 s45, s5, s23
	s_add_i32 s50, s50, s9
	s_lshl_b32 s9, s39, 13
	s_add_i32 s9, s18, s9
	s_add_i32 s56, s9, 0
	s_lshl_b32 s9, s41, 13
	v_mov_b32_e32 v2, 0
	s_add_i32 s13, s26, 0
	s_add_i32 s9, s20, s9
	v_lshlrev_b32_e32 v4, 4, v0
	v_mov_b32_e32 v5, v2
	s_mov_b32 m0, s13
	s_add_i32 s57, s9, 0
	s_lshl_b32 s9, s48, 8
	v_lshl_add_u64 v[138:139], s[44:45], 0, v[4:5]
	global_load_lds_dwordx4 v4, s[44:45]
	s_mov_b64 s[44:45], 0x2000
	s_add_i32 s51, s50, 0
	s_add_i32 s9, s9, 0
	v_and_b32_e32 v1, 63, v0
	v_lshl_add_u64 v[8:9], v[138:139], 0, s[44:45]
	s_add_i32 s44, s13, 0x8000
	s_ashr_i32 s17, s16, 31
	s_add_i32 s45, s51, 0x2000
	s_ashr_i32 s19, s18, 31
	s_add_i32 s46, s56, 0x2000
	s_ashr_i32 s21, s20, 31
	s_add_i32 s47, s57, 0x2000
	s_add_i32 s48, s9, 0x20000
	v_lshlrev_b32_e32 v6, 4, v1
	v_mov_b32_e32 v7, v2
	s_add_u32 s52, s2, s16
	s_mov_b32 m0, s44
	v_lshl_add_u64 v[140:141], s[2:3], 0, v[6:7]
	s_addc_u32 s53, s3, s17
	s_addk_i32 s51, 0x3800
	global_load_lds_dwordx4 v[8:9], off
	v_lshl_add_u64 v[8:9], v[140:141], 0, s[16:17]
	s_mov_b32 m0, s45
	v_lshl_add_u64 v[132:133], s[52:53], 0, v[6:7]
	s_add_u32 s52, s2, s18
	global_load_lds_dwordx4 v[8:9], off
	v_lshl_add_u64 v[8:9], v[140:141], 0, s[18:19]
	s_mov_b32 m0, s46
	s_addc_u32 s53, s3, s19
	global_load_lds_dwordx4 v[8:9], off
	v_lshl_add_u64 v[8:9], v[140:141], 0, s[20:21]
	s_mov_b32 m0, s47
	v_lshl_add_u64 v[134:135], s[52:53], 0, v[6:7]
	s_add_i32 s53, s56, 0x3800
	v_lshlrev_b32_e32 v130, 2, v0
	global_load_lds_dwordx4 v[8:9], off
	s_mov_b32 m0, s48
	s_mov_b64 s[54:55], 0x1800
	s_add_u32 s2, s2, s20
	global_load_lds_dword v130, s[14:15]
	v_lshl_add_u64 v[8:9], v[132:133], 0, s[54:55]
	s_mov_b32 m0, s51
	s_addc_u32 s3, s3, s21
	global_load_lds_dwordx4 v[8:9], off
	v_lshl_add_u64 v[8:9], v[134:135], 0, s[54:55]
	s_mov_b32 m0, s53
	v_lshl_add_u64 v[136:137], s[2:3], 0, v[6:7]
	global_load_lds_dwordx4 v[8:9], off
	v_lshl_add_u64 v[8:9], v[136:137], 0, s[54:55]
	s_add_i32 s54, s57, 0x3800
	s_mov_b32 m0, s54
	s_load_dwordx2 s[2:3], s[0:1], 0x20
	global_load_lds_dwordx4 v[8:9], off
	s_mov_b64 s[70:71], 0x4000
	s_add_i32 m0, s26, 0x10000
	v_lshl_add_u64 v[8:9], v[138:139], 0, s[70:71]
	global_load_lds_dwordx4 v[8:9], off
	s_mov_b64 s[70:71], 0x6000
	s_add_i32 m0, s13, 0x18000
	v_lshl_add_u64 v[8:9], v[138:139], 0, s[70:71]
	global_load_lds_dwordx4 v[8:9], off
	s_cmp_lg_u32 s27, 1
	v_mov_b32_e32 v131, v2
	s_cbranch_scc1 .LBB3_2
	s_barrier
